# attention fast loop: accumulator init taken directly from the constant -m block as MFMA SrcC (removes 23 VALU copies per 2 tiles)
# speedup vs baseline: 1.0062x; 1.0062x over previous
; #define AT_PK4(P, BASE, OUT) do { u32x4 w = {cvt_pk_bf16(P[BASE + 0], P[BASE + 1]), cvt_pk_bf16(P[BASE + 2], P[BASE + 3]), cvt_pk_bf16(P[BASE + 4], P[BASE + 5]), cvt_pk_bf16(P[BASE + 6], P[BASE + 7])}; \
;     OUT = *reinterpret_cast<bf16x8*>(&w); } while (0)
; __device__ __forceinline__ void finishFast(f32x16& p0, f32x16& p1, bool& ovf, float& l_reg, bf16x8& pa0, bf16x8& pa1, bf16x8& pa2, bf16x8& pa3) {
;     expSM(p1);
;     typedef float f32x2_t __attribute__((ext_vector_type(2)));
;     f32x2_t sa = {p0[0], p0[1]}, sb = {p0[8], p0[9]}, sc = {p1[0], p1[1]}, sd = {p1[8], p1[9]};
; #pragma unroll
;     for (int r = 2; r < 8; r += 2) { sa += f32x2_t{p0[r], p0[r + 1]}; sb += f32x2_t{p0[8 + r], p0[9 + r]}; sc += f32x2_t{p1[r], p1[r + 1]}; sd += f32x2_t{p1[8 + r], p1[9 + r]}; }
;     const f32x2_t ps2 = (sa + sb) + (sc + sd);
;     float ps = ps2.x + ps2.y;
;     { auto rr = __builtin_amdgcn_permlane32_swap(__float_as_uint(ps), __float_as_uint(ps), false, false);
;       ps = __uint_as_float(rr[0]) + __uint_as_float(rr[1]); }
;     l_reg += ps;
;     ...
;     AT_PK4(p0, 0, pa0); AT_PK4(p0, 8, pa1); AT_PK4(p1, 0, pa2); AT_PK4(p1, 8, pa3);
.LBB0_400:
	v_add_u32_e32 v67, s0, v171
	ds_read_b128 v[178:181], v67 offset:0
	ds_read_b128 v[182:185], v67 offset:0x1000
	v_add_u32_e32 v72, s0, v199
	ds_read_b128 v[186:189], v72 offset:0
	ds_read_b128 v[190:193], v72 offset:0x1000
	v_add_u32_e32 v73, s0, v200
	ds_read_b128 v[206:209], v73 offset:0
	ds_read_b128 v[210:213], v73 offset:0x1000
	v_exp_f32_e32 v222, v130
	v_add_u32_e32 v130, s0, v201
	ds_read_b128 v[214:217], v130 offset:0
	ds_read_b128 v[218:221], v130 offset:0x1000
	v_exp_f32_e32 v223, v131
	v_exp_f32_e32 v224, v132
	v_exp_f32_e32 v225, v133
	v_exp_f32_e32 v234, v134
	v_exp_f32_e32 v235, v135
	v_exp_f32_e32 v238, v136
	v_exp_f32_e32 v239, v137
	v_exp_f32_e32 v240, v138
	v_exp_f32_e32 v241, v139
	v_exp_f32_e32 v242, v140
	v_exp_f32_e32 v243, v141
	v_exp_f32_e32 v244, v142
	v_exp_f32_e32 v245, v143
	v_exp_f32_e32 v246, v144
	v_exp_f32_e32 v247, v145
	v_mfma_f32_32x32x16_bf16 v[50:65], v[68:71], v[164:167], v[50:65]
	v_mfma_f32_32x32x16_bf16 v[50:65], v[78:81], v[110:113], v[50:65]
	s_waitcnt lgkmcnt(6)
	s_waitcnt lgkmcnt(4)
	s_waitcnt lgkmcnt(2)
	v_mfma_f32_32x32x16_bf16 v[50:65], v[74:77], v[106:109], v[50:65]
	s_waitcnt lgkmcnt(0)
	v_mfma_f32_32x32x16_bf16 v[50:65], v[98:101], v[102:105], v[50:65]
	v_mfma_f32_32x32x16_bf16 v[130:145], v[178:181], v[148:151], v[82:97]
	v_exp_f32_e32 v76, v114
	v_exp_f32_e32 v77, v115
	v_exp_f32_e32 v78, v116
	v_exp_f32_e32 v79, v117
	v_exp_f32_e32 v80, v118
	v_exp_f32_e32 v81, v119
	v_exp_f32_e32 v116, v122
	v_mfma_f32_32x32x16_bf16 v[98:113], v[182:185], v[148:151], v[82:97]
	v_exp_f32_e32 v117, v123
	v_exp_f32_e32 v118, v124
	v_exp_f32_e32 v119, v125
	v_exp_f32_e32 v114, v120
	v_exp_f32_e32 v115, v121
	v_exp_f32_e32 v120, v126
	v_exp_f32_e32 v121, v127
	v_mfma_f32_32x32x16_bf16 v[130:145], v[186:189], v[152:155], v[130:145]
	v_exp_f32_e32 v122, v128
	v_exp_f32_e32 v123, v129
	v_pk_add_f32 v[68:69], v[222:223], v[224:225]
	v_pk_add_f32 v[70:71], v[240:241], v[242:243]
	v_pk_add_f32 v[72:73], v[78:79], v[76:77]
	v_pk_add_f32 v[74:75], v[118:119], v[116:117]
	v_pk_add_f32 v[68:69], v[234:235], v[68:69]
	v_mfma_f32_32x32x16_bf16 v[98:113], v[190:193], v[152:155], v[98:113]
	v_add_f32_e64 v70, v244, v70
	v_add_f32_e64 v71, v245, v71
	v_add_f32_e64 v72, v80, v72
	v_add_f32_e64 v73, v81, v73
	v_add_f32_e64 v74, v120, v74
	v_add_f32_e64 v75, v121, v75
	v_pk_add_f32 v[68:69], v[238:239], v[68:69]
	v_pk_add_f32 v[70:71], v[246:247], v[70:71]
	v_pk_add_f32 v[72:73], v[114:115], v[72:73]
	v_pk_add_f32 v[74:75], v[122:123], v[74:75]
	v_mfma_f32_32x32x16_bf16 v[130:145], v[206:209], v[156:159], v[130:145]
	v_add_f32_e64 v68, v68, v70
	v_add_f32_e64 v69, v69, v71
	v_add_f32_e64 v70, v72, v74
	v_add_f32_e64 v71, v73, v75
	v_add_f32_e64 v68, v68, v70
	v_add_f32_e64 v69, v69, v71
	v_pk_add_f32 v[192:193], v[68:69], v[68:69] op_sel:[0,1] op_sel_hi:[1,0]
	v_cvt_pk_bf16_f32 v68, v222, v223
	v_mfma_f32_32x32x16_bf16 v[98:113], v[210:213], v[156:159], v[98:113]
	v_mov_b32_e32 v67, v192
	s_nop 1
	v_permlane32_swap_b32_e32 v192, v67
	v_cvt_pk_bf16_f32 v69, v224, v225
	v_cvt_pk_bf16_f32 v70, v234, v235
	v_cvt_pk_bf16_f32 v71, v238, v239
	v_cvt_pk_bf16_f32 v72, v240, v241
	v_mfma_f32_32x32x16_bf16 v[130:145], v[214:217], v[160:163], v[130:145]
	v_cvt_pk_bf16_f32 v73, v242, v243
	v_cvt_pk_bf16_f32 v74, v244, v245
	v_cvt_pk_bf16_f32 v75, v246, v247
	v_cvt_pk_bf16_f32 v76, v76, v77
	v_cvt_pk_bf16_f32 v77, v78, v79
	v_cvt_pk_bf16_f32 v78, v80, v81
	v_cvt_pk_bf16_f32 v79, v114, v115
	v_mfma_f32_32x32x16_bf16 v[98:113], v[218:221], v[160:163], v[98:113]
	v_cvt_pk_bf16_f32 v114, v116, v117
	v_cvt_pk_bf16_f32 v115, v118, v119
	v_cvt_pk_bf16_f32 v116, v120, v121
	v_cvt_pk_bf16_f32 v117, v122, v123
	s_and_b64 vcc, exec, s[42:43]
	s_cbranch_vccnz .LBB0_409
	s_cmp_ge_u32 s2, s74
	s_mov_b64 s[8:9], -1
	s_cbranch_scc0 .LBB0_403
	s_waitcnt vmcnt(0) lgkmcnt(0)
	s_mov_b64 s[8:9], 0
